# g2p + phase 0 W_xq conversion loop: 4 iterations unrolled, all 12 loads issued up front with counted waits
# baseline (speedup 1.0000x reference)
; __device__ __forceinline__ unsigned pk2(float lo, float hi) { return f2bf(lo) | (f2bf(hi) << 16); }
; #define INP(k) ldptr(PTAB, (k))
; __global__ void __launch_bounds__(NWAVES * 64, 2) fwd_kernel(Args args) {
;     ...
;             { const float* wq = INP(19) + (size_t)l * D * D; const float* gq = INP(17) + l * D;
;               for (int i = gw * 64 + lane; i < D * D / 8; i += ngw * 64) { const f32x4 a = *(const f32x4*)(wq + (size_t)i * 8), bq = *(const f32x4*)(wq + (size_t)i * 8 + 4); const float gg = gq[i >> 8];
;                   v4u o; o.x = pk2(a.x * gg, a.y * gg); o.y = pk2(a.z * gg, a.w * gg); o.z = pk2(bq.x * gg, bq.y * gg); o.w = pk2(bq.z * gg, bq.w * gg); ((v4u*)WSP(WS_WXQ))[i] = o; } }
.LBB0_490:
	v_ashrrev_i32_e32 v60, 8, v0
	v_ashrrev_i32_e32 v61, 31, v60
	global_load_dwordx4 v[40:43], v[4:5], off offset:-16
	global_load_dwordx4 v[80:83], v[4:5], off
	v_lshl_add_u64 v[60:61], v[60:61], 2, s[4:5]
	global_load_dword v56, v[60:61], off
	v_add_u32_e32 v0, s82, v0
	v_lshl_add_u64 v[4:5], v[4:5], 0, s[88:89]
	v_ashrrev_i32_e32 v60, 8, v0
	v_ashrrev_i32_e32 v61, 31, v60
	global_load_dwordx4 v[44:47], v[4:5], off offset:-16
	global_load_dwordx4 v[84:87], v[4:5], off
	v_lshl_add_u64 v[60:61], v[60:61], 2, s[4:5]
	global_load_dword v57, v[60:61], off
	v_add_u32_e32 v0, s82, v0
	v_lshl_add_u64 v[4:5], v[4:5], 0, s[88:89]
	v_ashrrev_i32_e32 v60, 8, v0
	v_ashrrev_i32_e32 v61, 31, v60
	global_load_dwordx4 v[48:51], v[4:5], off offset:-16
	global_load_dwordx4 v[88:91], v[4:5], off
	v_lshl_add_u64 v[60:61], v[60:61], 2, s[4:5]
	global_load_dword v58, v[60:61], off
	v_add_u32_e32 v0, s82, v0
	v_lshl_add_u64 v[4:5], v[4:5], 0, s[88:89]
	v_ashrrev_i32_e32 v60, 8, v0
	v_ashrrev_i32_e32 v61, 31, v60
	global_load_dwordx4 v[52:55], v[4:5], off offset:-16
	global_load_dwordx4 v[92:95], v[4:5], off
	v_lshl_add_u64 v[60:61], v[60:61], 2, s[4:5]
	global_load_dword v59, v[60:61], off
	v_add_u32_e32 v0, s82, v0
	v_lshl_add_u64 v[4:5], v[4:5], 0, s[88:89]
	s_waitcnt vmcnt(9)
	v_mov_b32_e32 v6, v40
	v_mov_b32_e32 v7, v41
	v_mov_b32_e32 v8, v42
	v_mov_b32_e32 v9, v43
	v_mov_b32_e32 v10, v80
	v_mov_b32_e32 v11, v81
	v_mov_b32_e32 v12, v82
	v_mov_b32_e32 v13, v83
	v_mov_b32_e32 v14, v56
	v_mov_b32_e32 v16, v6
	v_mov_b32_e32 v17, v8
	v_mov_b32_e32 v8, v7
	v_mov_b32_e32 v6, v10
	v_mov_b32_e32 v7, v12
	v_mov_b32_e32 v12, v11
	v_pk_mul_f32 v[10:11], v[16:17], v[14:15] op_sel_hi:[1,0]
	v_pk_mul_f32 v[6:7], v[6:7], v[14:15] op_sel_hi:[1,0]
	v_pk_mul_f32 v[8:9], v[8:9], v[14:15] op_sel_hi:[1,0]
	v_pk_mul_f32 v[12:13], v[12:13], v[14:15] op_sel_hi:[1,0]
	v_bfe_u32 v18, v10, 16, 1
	v_bfe_u32 v19, v11, 16, 1
	v_bfe_u32 v20, v6, 16, 1
	v_bfe_u32 v21, v7, 16, 1
	v_bfe_u32 v14, v13, 16, 1
	v_bfe_u32 v15, v12, 16, 1
	v_bfe_u32 v16, v9, 16, 1
	v_bfe_u32 v17, v8, 16, 1
	v_add3_u32 v7, v7, v21, s40
	v_add3_u32 v6, v6, v20, s40
	v_add3_u32 v11, v11, v19, s40
	v_add3_u32 v10, v10, v18, s40
	v_add3_u32 v17, v8, v17, s40
	v_add3_u32 v16, v9, v16, s40
	v_add3_u32 v8, v12, v15, s40
	v_add3_u32 v9, v13, v14, s40
	v_lshrrev_b32_e32 v10, 16, v10
	v_lshrrev_b32_e32 v11, 16, v11
	v_lshrrev_b32_e32 v6, 16, v6
	v_lshrrev_b32_e32 v7, 16, v7
	v_and_or_b32 v9, v9, s41, v7
	v_and_or_b32 v8, v8, s41, v6
	v_and_or_b32 v7, v16, s41, v11
	v_and_or_b32 v6, v17, s41, v10
	global_store_dwordx4 v[2:3], v[6:9], off
	v_lshl_add_u64 v[2:3], v[2:3], 0, s[86:87]
	s_nop 1
	s_waitcnt vmcnt(6)
	v_mov_b32_e32 v6, v44
	v_mov_b32_e32 v7, v45
	v_mov_b32_e32 v8, v46
	v_mov_b32_e32 v9, v47
	v_mov_b32_e32 v10, v84
	v_mov_b32_e32 v11, v85
	v_mov_b32_e32 v12, v86
	v_mov_b32_e32 v13, v87
	v_mov_b32_e32 v14, v57
	v_mov_b32_e32 v16, v6
	v_mov_b32_e32 v17, v8
	v_mov_b32_e32 v8, v7
	v_mov_b32_e32 v6, v10
	v_mov_b32_e32 v7, v12
	v_mov_b32_e32 v12, v11
	v_pk_mul_f32 v[10:11], v[16:17], v[14:15] op_sel_hi:[1,0]
	v_pk_mul_f32 v[6:7], v[6:7], v[14:15] op_sel_hi:[1,0]
	v_pk_mul_f32 v[8:9], v[8:9], v[14:15] op_sel_hi:[1,0]
	v_pk_mul_f32 v[12:13], v[12:13], v[14:15] op_sel_hi:[1,0]
	v_bfe_u32 v18, v10, 16, 1
	v_bfe_u32 v19, v11, 16, 1
	v_bfe_u32 v20, v6, 16, 1
	v_bfe_u32 v21, v7, 16, 1
	v_bfe_u32 v14, v13, 16, 1
	v_bfe_u32 v15, v12, 16, 1
	v_bfe_u32 v16, v9, 16, 1
	v_bfe_u32 v17, v8, 16, 1
	v_add3_u32 v7, v7, v21, s40
	v_add3_u32 v6, v6, v20, s40
	v_add3_u32 v11, v11, v19, s40
	v_add3_u32 v10, v10, v18, s40
	v_add3_u32 v17, v8, v17, s40
	v_add3_u32 v16, v9, v16, s40
	v_add3_u32 v8, v12, v15, s40
	v_add3_u32 v9, v13, v14, s40
	v_lshrrev_b32_e32 v10, 16, v10
	v_lshrrev_b32_e32 v11, 16, v11
	v_lshrrev_b32_e32 v6, 16, v6
	v_lshrrev_b32_e32 v7, 16, v7
	v_and_or_b32 v9, v9, s41, v7
	v_and_or_b32 v8, v8, s41, v6
	v_and_or_b32 v7, v16, s41, v11
	v_and_or_b32 v6, v17, s41, v10
	global_store_dwordx4 v[2:3], v[6:9], off
	v_lshl_add_u64 v[2:3], v[2:3], 0, s[86:87]
	s_nop 1
	s_waitcnt vmcnt(3)
	v_mov_b32_e32 v6, v48
	v_mov_b32_e32 v7, v49
	v_mov_b32_e32 v8, v50
	v_mov_b32_e32 v9, v51
	v_mov_b32_e32 v10, v88
	v_mov_b32_e32 v11, v89
	v_mov_b32_e32 v12, v90
	v_mov_b32_e32 v13, v91
	v_mov_b32_e32 v14, v58
	v_mov_b32_e32 v16, v6
	v_mov_b32_e32 v17, v8
	v_mov_b32_e32 v8, v7
	v_mov_b32_e32 v6, v10
	v_mov_b32_e32 v7, v12
	v_mov_b32_e32 v12, v11
	v_pk_mul_f32 v[10:11], v[16:17], v[14:15] op_sel_hi:[1,0]
	v_pk_mul_f32 v[6:7], v[6:7], v[14:15] op_sel_hi:[1,0]
	v_pk_mul_f32 v[8:9], v[8:9], v[14:15] op_sel_hi:[1,0]
	v_pk_mul_f32 v[12:13], v[12:13], v[14:15] op_sel_hi:[1,0]
	v_bfe_u32 v18, v10, 16, 1
	v_bfe_u32 v19, v11, 16, 1
	v_bfe_u32 v20, v6, 16, 1
	v_bfe_u32 v21, v7, 16, 1
	v_bfe_u32 v14, v13, 16, 1
	v_bfe_u32 v15, v12, 16, 1
	v_bfe_u32 v16, v9, 16, 1
	v_bfe_u32 v17, v8, 16, 1
	v_add3_u32 v7, v7, v21, s40
	v_add3_u32 v6, v6, v20, s40
	v_add3_u32 v11, v11, v19, s40
	v_add3_u32 v10, v10, v18, s40
	v_add3_u32 v17, v8, v17, s40
	v_add3_u32 v16, v9, v16, s40
	v_add3_u32 v8, v12, v15, s40
	v_add3_u32 v9, v13, v14, s40
	v_lshrrev_b32_e32 v10, 16, v10
	v_lshrrev_b32_e32 v11, 16, v11
	v_lshrrev_b32_e32 v6, 16, v6
	v_lshrrev_b32_e32 v7, 16, v7
	v_and_or_b32 v9, v9, s41, v7
	v_and_or_b32 v8, v8, s41, v6
	v_and_or_b32 v7, v16, s41, v11
	v_and_or_b32 v6, v17, s41, v10
	global_store_dwordx4 v[2:3], v[6:9], off
	v_lshl_add_u64 v[2:3], v[2:3], 0, s[86:87]
	s_nop 1
	s_waitcnt vmcnt(0)
	v_mov_b32_e32 v6, v52
	v_mov_b32_e32 v7, v53
	v_mov_b32_e32 v8, v54
	v_mov_b32_e32 v9, v55
	v_mov_b32_e32 v10, v92
	v_mov_b32_e32 v11, v93
	v_mov_b32_e32 v12, v94
	v_mov_b32_e32 v13, v95
	v_mov_b32_e32 v14, v59
	v_mov_b32_e32 v16, v6
	v_mov_b32_e32 v17, v8
	v_mov_b32_e32 v8, v7
	v_mov_b32_e32 v6, v10
	v_mov_b32_e32 v7, v12
	v_mov_b32_e32 v12, v11
	v_pk_mul_f32 v[10:11], v[16:17], v[14:15] op_sel_hi:[1,0]
	v_pk_mul_f32 v[6:7], v[6:7], v[14:15] op_sel_hi:[1,0]
	v_pk_mul_f32 v[8:9], v[8:9], v[14:15] op_sel_hi:[1,0]
	v_pk_mul_f32 v[12:13], v[12:13], v[14:15] op_sel_hi:[1,0]
	v_bfe_u32 v18, v10, 16, 1
	v_bfe_u32 v19, v11, 16, 1
	v_bfe_u32 v20, v6, 16, 1
	v_bfe_u32 v21, v7, 16, 1
	v_bfe_u32 v14, v13, 16, 1
	v_bfe_u32 v15, v12, 16, 1
	v_bfe_u32 v16, v9, 16, 1
	v_bfe_u32 v17, v8, 16, 1
	v_add3_u32 v7, v7, v21, s40
	v_add3_u32 v6, v6, v20, s40
	v_add3_u32 v11, v11, v19, s40
	v_add3_u32 v10, v10, v18, s40
	v_add3_u32 v17, v8, v17, s40
	v_add3_u32 v16, v9, v16, s40
	v_add3_u32 v8, v12, v15, s40
	v_add3_u32 v9, v13, v14, s40
	v_lshrrev_b32_e32 v10, 16, v10
	v_lshrrev_b32_e32 v11, 16, v11
	v_lshrrev_b32_e32 v6, 16, v6
	v_lshrrev_b32_e32 v7, 16, v7
	v_and_or_b32 v9, v9, s41, v7
	v_and_or_b32 v8, v8, s41, v6
	v_and_or_b32 v7, v16, s41, v11
	v_and_or_b32 v6, v17, s41, v10
	global_store_dwordx4 v[2:3], v[6:9], off
	v_lshl_add_u64 v[2:3], v[2:3], 0, s[86:87]
